# gate-projection fp8 outputs stored non-temporal (read three phases later)
# speedup vs baseline: 1.0114x; 1.0114x over previous
.LBB0_419:
	ds_read_b128 v[10:13], v130
	ds_read_b128 v[14:17], v130 offset:1024
	ds_read_b128 v[160:163], v130 offset:2048
	ds_read_b128 v[164:167], v130 offset:3072
	s_add_u32 s68, s66, 0xfffe0080
	s_addc_u32 s69, s67, -1
	s_cmp_eq_u32 s76, 4
	s_cselect_b32 s71, s19, s69
	s_cselect_b32 s70, s18, s68
	s_cselect_b32 s69, s65, s75
	s_cselect_b32 s68, s64, s74
	s_mov_b32 m0, s9
	v_lshl_add_u64 v[2:3], s[66:67], 0, v[156:157]
	ds_read_b128 v[178:181], v170
	ds_read_b128 v[182:185], v170 offset:1024
	ds_read_b128 v[186:189], v170 offset:2048
	ds_read_b128 v[190:193], v170 offset:3072
	ds_read_b128 v[194:197], v170 offset:4096
	ds_read_b128 v[198:201], v170 offset:5120
	ds_read_b128 v[218:221], v170 offset:6144
	ds_read_b128 v[222:225], v170 offset:7168
	global_load_lds_dwordx4 v[2:3], off
	v_lshl_add_u64 v[2:3], s[66:67], 0, v[158:159]
	s_mov_b32 m0, s51
	s_nop 0
	global_load_lds_dwordx4 v[2:3], off
	s_waitcnt lgkmcnt(8)
	s_waitcnt vmcnt(10)
	s_barrier
	s_setprio 1
	s_waitcnt lgkmcnt(6)
	v_mfma_scale_f32_16x16x128_f8f6f4 v[136:139], v[10:17], v[178:185], v[136:139], v205, v205 op_sel_hi:[0,0,0]
	v_mfma_scale_f32_16x16x128_f8f6f4 v[132:135], v[160:167], v[178:185], v[132:135], v205, v205 op_sel_hi:[0,0,0]
	s_waitcnt lgkmcnt(4)
	v_mfma_scale_f32_16x16x128_f8f6f4 v[118:121], v[10:17], v[186:193], v[118:121], v205, v205 op_sel_hi:[0,0,0]
	v_mfma_scale_f32_16x16x128_f8f6f4 v[114:117], v[160:167], v[186:193], v[114:117], v205, v205 op_sel_hi:[0,0,0]
	s_waitcnt lgkmcnt(2)
	v_mfma_scale_f32_16x16x128_f8f6f4 v[106:109], v[10:17], v[194:201], v[106:109], v205, v205 op_sel_hi:[0,0,0]
	v_mfma_scale_f32_16x16x128_f8f6f4 v[98:101], v[160:167], v[194:201], v[98:101], v205, v205 op_sel_hi:[0,0,0]
	s_waitcnt lgkmcnt(0)
	v_mfma_scale_f32_16x16x128_f8f6f4 v[86:89], v[10:17], v[218:225], v[86:89], v205, v205 op_sel_hi:[0,0,0]
	v_mfma_scale_f32_16x16x128_f8f6f4 v[70:73], v[160:167], v[218:225], v[70:73], v205, v205 op_sel_hi:[0,0,0]
	s_setprio 0
	s_barrier
	s_mov_b32 m0, s58
	v_lshl_add_u64 v[6:7], s[68:69], 0, v[154:155]
	ds_read_b128 v[226:229], v171
	ds_read_b128 v[230:233], v171 offset:1024
	ds_read_b128 v[234:237], v171 offset:2048
	ds_read_b128 v[238:241], v171 offset:3072
	global_load_lds_dwordx4 v[6:7], off
	v_lshl_add_u64 v[8:9], s[68:69], 0, v[150:151]
	s_mov_b32 m0, s59
	s_nop 0
	global_load_lds_dwordx4 v[8:9], off
	s_waitcnt vmcnt(10)
	s_barrier
	s_setprio 1
	s_waitcnt lgkmcnt(2)
	v_mfma_scale_f32_16x16x128_f8f6f4 v[144:147], v[226:233], v[178:185], v[144:147], v205, v205 op_sel_hi:[0,0,0]
	s_waitcnt lgkmcnt(0)
	v_mfma_scale_f32_16x16x128_f8f6f4 v[140:143], v[234:241], v[178:185], v[140:143], v205, v205 op_sel_hi:[0,0,0]
	v_mfma_scale_f32_16x16x128_f8f6f4 v[126:129], v[226:233], v[186:193], v[126:129], v205, v205 op_sel_hi:[0,0,0]
	v_mfma_scale_f32_16x16x128_f8f6f4 v[122:125], v[234:241], v[186:193], v[122:125], v205, v205 op_sel_hi:[0,0,0]
	v_mfma_scale_f32_16x16x128_f8f6f4 v[110:113], v[226:233], v[194:201], v[110:113], v205, v205 op_sel_hi:[0,0,0]
	v_mfma_scale_f32_16x16x128_f8f6f4 v[102:105], v[234:241], v[194:201], v[102:105], v205, v205 op_sel_hi:[0,0,0]
	v_mfma_scale_f32_16x16x128_f8f6f4 v[94:97], v[226:233], v[218:225], v[94:97], v205, v205 op_sel_hi:[0,0,0]
	v_mfma_scale_f32_16x16x128_f8f6f4 v[78:81], v[234:241], v[218:225], v[78:81], v205, v205 op_sel_hi:[0,0,0]
	s_setprio 0
	s_mov_b32 m0, s39
	v_lshl_add_u64 v[2:3], s[70:71], 0, v[152:153]
	s_barrier
	ds_read_b128 v[178:181], v170 offset:16384
	ds_read_b128 v[182:185], v170 offset:17408
	ds_read_b128 v[186:189], v170 offset:18432
	ds_read_b128 v[190:193], v170 offset:19456
	ds_read_b128 v[194:197], v170 offset:20480
	ds_read_b128 v[198:201], v170 offset:21504
	ds_read_b128 v[218:221], v170 offset:22528
	ds_read_b128 v[222:225], v170 offset:23552
	global_load_lds_dwordx4 v[2:3], off
	v_lshl_add_u64 v[4:5], s[70:71], 0, v[148:149]
	s_mov_b32 m0, s42
	s_nop 0
	global_load_lds_dwordx4 v[4:5], off
	s_barrier
	s_setprio 1
	s_waitcnt lgkmcnt(6)
	v_mfma_scale_f32_16x16x128_f8f6f4 v[82:85], v[10:17], v[178:185], v[82:85], v205, v205 op_sel_hi:[0,0,0]
	v_mfma_scale_f32_16x16x128_f8f6f4 v[66:69], v[160:167], v[178:185], v[66:69], v205, v205 op_sel_hi:[0,0,0]
	s_waitcnt lgkmcnt(4)
	v_mfma_scale_f32_16x16x128_f8f6f4 v[58:61], v[10:17], v[186:193], v[58:61], v205, v205 op_sel_hi:[0,0,0]
	v_mfma_scale_f32_16x16x128_f8f6f4 v[50:53], v[160:167], v[186:193], v[50:53], v205, v205 op_sel_hi:[0,0,0]
	s_waitcnt lgkmcnt(2)
	v_mfma_scale_f32_16x16x128_f8f6f4 v[46:49], v[10:17], v[194:201], v[46:49], v205, v205 op_sel_hi:[0,0,0]
	v_mfma_scale_f32_16x16x128_f8f6f4 v[38:41], v[160:167], v[194:201], v[38:41], v205, v205 op_sel_hi:[0,0,0]
	s_waitcnt lgkmcnt(0)
	v_mfma_scale_f32_16x16x128_f8f6f4 v[30:33], v[10:17], v[218:225], v[30:33], v205, v205 op_sel_hi:[0,0,0]
	v_mfma_scale_f32_16x16x128_f8f6f4 v[22:25], v[160:167], v[218:225], v[22:25], v205, v205 op_sel_hi:[0,0,0]
	s_setprio 0
	s_barrier
	s_add_u32 s78, s68, 0x2000
	s_addc_u32 s79, s69, 0
	s_mov_b32 m0, s60
	v_lshl_add_u64 v[10:11], s[78:79], 0, v[154:155]
	global_load_lds_dwordx4 v[10:11], off
	v_lshl_add_u64 v[10:11], s[78:79], 0, v[150:151]
	s_mov_b32 m0, s61
	s_nop 0
	global_load_lds_dwordx4 v[10:11], off
	s_waitcnt vmcnt(10)
	s_barrier
	s_setprio 1
	v_mfma_scale_f32_16x16x128_f8f6f4 v[90:93], v[226:233], v[178:185], v[90:93], v205, v205 op_sel_hi:[0,0,0]
	v_mfma_scale_f32_16x16x128_f8f6f4 v[74:77], v[234:241], v[178:185], v[74:77], v205, v205 op_sel_hi:[0,0,0]
	v_mfma_scale_f32_16x16x128_f8f6f4 v[62:65], v[226:233], v[186:193], v[62:65], v205, v205 op_sel_hi:[0,0,0]
	v_mfma_scale_f32_16x16x128_f8f6f4 v[54:57], v[234:241], v[186:193], v[54:57], v205, v205 op_sel_hi:[0,0,0]
	v_mfma_scale_f32_16x16x128_f8f6f4 v[42:45], v[226:233], v[194:201], v[42:45], v205, v205 op_sel_hi:[0,0,0]
	v_mfma_scale_f32_16x16x128_f8f6f4 v[34:37], v[234:241], v[194:201], v[34:37], v205, v205 op_sel_hi:[0,0,0]
	v_mfma_scale_f32_16x16x128_f8f6f4 v[26:29], v[226:233], v[218:225], v[26:29], v205, v205 op_sel_hi:[0,0,0]
	v_mfma_scale_f32_16x16x128_f8f6f4 v[18:21], v[234:241], v[218:225], v[18:21], v205, v205 op_sel_hi:[0,0,0]
	s_setprio 0
	s_barrier
	ds_read_b128 v[10:13], v172
	ds_read_b128 v[14:17], v172 offset:1024
	ds_read_b128 v[160:163], v172 offset:2048
	ds_read_b128 v[164:167], v172 offset:3072
	s_add_u32 s70, s70, 0x20000
	s_addc_u32 s71, s71, 0
	s_mov_b32 m0, s43
	v_lshl_add_u64 v[174:175], s[70:71], 0, v[152:153]
	ds_read_b128 v[178:181], v170 offset:32768
	ds_read_b128 v[182:185], v170 offset:33792
	ds_read_b128 v[186:189], v170 offset:34816
	ds_read_b128 v[190:193], v170 offset:35840
	ds_read_b128 v[194:197], v170 offset:36864
	ds_read_b128 v[198:201], v170 offset:37888
	ds_read_b128 v[218:221], v170 offset:38912
	ds_read_b128 v[222:225], v170 offset:39936
	global_load_lds_dwordx4 v[174:175], off
	v_lshl_add_u64 v[174:175], s[70:71], 0, v[148:149]
	s_mov_b32 m0, s44
	s_nop 0
	global_load_lds_dwordx4 v[174:175], off
	s_waitcnt lgkmcnt(8)
	s_waitcnt vmcnt(10)
	s_barrier
	s_setprio 1
	s_waitcnt lgkmcnt(6)
	v_mfma_scale_f32_16x16x128_f8f6f4 v[136:139], v[10:17], v[178:185], v[136:139], v205, v205 op_sel_hi:[0,0,0]
	v_mfma_scale_f32_16x16x128_f8f6f4 v[132:135], v[160:167], v[178:185], v[132:135], v205, v205 op_sel_hi:[0,0,0]
	s_waitcnt lgkmcnt(4)
	v_mfma_scale_f32_16x16x128_f8f6f4 v[118:121], v[10:17], v[186:193], v[118:121], v205, v205 op_sel_hi:[0,0,0]
	v_mfma_scale_f32_16x16x128_f8f6f4 v[114:117], v[160:167], v[186:193], v[114:117], v205, v205 op_sel_hi:[0,0,0]
	s_waitcnt lgkmcnt(2)
	v_mfma_scale_f32_16x16x128_f8f6f4 v[106:109], v[10:17], v[194:201], v[106:109], v205, v205 op_sel_hi:[0,0,0]
	v_mfma_scale_f32_16x16x128_f8f6f4 v[98:101], v[160:167], v[194:201], v[98:101], v205, v205 op_sel_hi:[0,0,0]
	s_waitcnt lgkmcnt(0)
	v_mfma_scale_f32_16x16x128_f8f6f4 v[86:89], v[10:17], v[218:225], v[86:89], v205, v205 op_sel_hi:[0,0,0]
	v_mfma_scale_f32_16x16x128_f8f6f4 v[70:73], v[160:167], v[218:225], v[70:73], v205, v205 op_sel_hi:[0,0,0]
	s_setprio 0
	s_barrier
	s_mov_b32 m0, s62
	v_lshl_add_u64 v[6:7], v[6:7], 0, s[30:31]
	ds_read_b128 v[226:229], v173
	ds_read_b128 v[230:233], v173 offset:1024
	ds_read_b128 v[234:237], v173 offset:2048
	ds_read_b128 v[238:241], v173 offset:3072
	global_load_lds_dwordx4 v[6:7], off
	v_lshl_add_u64 v[6:7], v[8:9], 0, s[30:31]
	s_mov_b32 m0, s63
	s_nop 0
	global_load_lds_dwordx4 v[6:7], off
	s_waitcnt vmcnt(10)
	s_barrier
	s_setprio 1
	s_waitcnt lgkmcnt(2)
	v_mfma_scale_f32_16x16x128_f8f6f4 v[144:147], v[226:233], v[178:185], v[144:147], v205, v205 op_sel_hi:[0,0,0]
	s_waitcnt lgkmcnt(0)
	v_mfma_scale_f32_16x16x128_f8f6f4 v[140:143], v[234:241], v[178:185], v[140:143], v205, v205 op_sel_hi:[0,0,0]
	v_mfma_scale_f32_16x16x128_f8f6f4 v[126:129], v[226:233], v[186:193], v[126:129], v205, v205 op_sel_hi:[0,0,0]
	v_mfma_scale_f32_16x16x128_f8f6f4 v[122:125], v[234:241], v[186:193], v[122:125], v205, v205 op_sel_hi:[0,0,0]
	v_mfma_scale_f32_16x16x128_f8f6f4 v[110:113], v[226:233], v[194:201], v[110:113], v205, v205 op_sel_hi:[0,0,0]
	v_mfma_scale_f32_16x16x128_f8f6f4 v[102:105], v[234:241], v[194:201], v[102:105], v205, v205 op_sel_hi:[0,0,0]
	v_mfma_scale_f32_16x16x128_f8f6f4 v[94:97], v[226:233], v[218:225], v[94:97], v205, v205 op_sel_hi:[0,0,0]
	v_mfma_scale_f32_16x16x128_f8f6f4 v[78:81], v[234:241], v[218:225], v[78:81], v205, v205 op_sel_hi:[0,0,0]
	s_setprio 0
	s_mov_b32 m0, s45
	v_lshl_add_u64 v[2:3], v[2:3], 0, s[30:31]
	s_barrier
	ds_read_b128 v[178:181], v170 offset:49152
	ds_read_b128 v[182:185], v170 offset:50176
	ds_read_b128 v[186:189], v170 offset:51200
	ds_read_b128 v[190:193], v170 offset:52224
	ds_read_b128 v[194:197], v170 offset:53248
	ds_read_b128 v[198:201], v170 offset:54272
	ds_read_b128 v[218:221], v170 offset:55296
	ds_read_b128 v[222:225], v170 offset:56320
	global_load_lds_dwordx4 v[2:3], off
	v_lshl_add_u64 v[2:3], v[4:5], 0, s[30:31]
	s_mov_b32 m0, s46
	s_nop 0
	global_load_lds_dwordx4 v[2:3], off
	s_barrier
	s_setprio 1
	s_waitcnt lgkmcnt(6)
	v_mfma_scale_f32_16x16x128_f8f6f4 v[82:85], v[10:17], v[178:185], v[82:85], v205, v205 op_sel_hi:[0,0,0]
	v_mfma_scale_f32_16x16x128_f8f6f4 v[66:69], v[160:167], v[178:185], v[66:69], v205, v205 op_sel_hi:[0,0,0]
	s_waitcnt lgkmcnt(4)
	v_mfma_scale_f32_16x16x128_f8f6f4 v[58:61], v[10:17], v[186:193], v[58:61], v205, v205 op_sel_hi:[0,0,0]
	v_mfma_scale_f32_16x16x128_f8f6f4 v[50:53], v[160:167], v[186:193], v[50:53], v205, v205 op_sel_hi:[0,0,0]
	s_waitcnt lgkmcnt(2)
	v_mfma_scale_f32_16x16x128_f8f6f4 v[46:49], v[10:17], v[194:201], v[46:49], v205, v205 op_sel_hi:[0,0,0]
	v_mfma_scale_f32_16x16x128_f8f6f4 v[38:41], v[160:167], v[194:201], v[38:41], v205, v205 op_sel_hi:[0,0,0]
	s_waitcnt lgkmcnt(0)
	v_mfma_scale_f32_16x16x128_f8f6f4 v[30:33], v[10:17], v[218:225], v[30:33], v205, v205 op_sel_hi:[0,0,0]
	v_mfma_scale_f32_16x16x128_f8f6f4 v[22:25], v[160:167], v[218:225], v[22:25], v205, v205 op_sel_hi:[0,0,0]
	s_setprio 0
	s_barrier
	s_add_u32 s68, s68, 0x2080
	s_addc_u32 s69, s69, 0
	s_mov_b32 m0, s72
	v_lshl_add_u64 v[2:3], s[68:69], 0, v[154:155]
	global_load_lds_dwordx4 v[2:3], off
	v_lshl_add_u64 v[2:3], s[68:69], 0, v[150:151]
	s_mov_b32 m0, s73
	s_nop 0
	global_load_lds_dwordx4 v[2:3], off
	s_waitcnt vmcnt(10)
	s_barrier
	s_setprio 1
	v_mfma_scale_f32_16x16x128_f8f6f4 v[90:93], v[226:233], v[178:185], v[90:93], v205, v205 op_sel_hi:[0,0,0]
	v_mfma_scale_f32_16x16x128_f8f6f4 v[74:77], v[234:241], v[178:185], v[74:77], v205, v205 op_sel_hi:[0,0,0]
	v_mfma_scale_f32_16x16x128_f8f6f4 v[62:65], v[226:233], v[186:193], v[62:65], v205, v205 op_sel_hi:[0,0,0]
	v_mfma_scale_f32_16x16x128_f8f6f4 v[54:57], v[234:241], v[186:193], v[54:57], v205, v205 op_sel_hi:[0,0,0]
	v_mfma_scale_f32_16x16x128_f8f6f4 v[42:45], v[226:233], v[194:201], v[42:45], v205, v205 op_sel_hi:[0,0,0]
	v_mfma_scale_f32_16x16x128_f8f6f4 v[34:37], v[234:241], v[194:201], v[34:37], v205, v205 op_sel_hi:[0,0,0]
	v_mfma_scale_f32_16x16x128_f8f6f4 v[26:29], v[226:233], v[218:225], v[26:29], v205, v205 op_sel_hi:[0,0,0]
	v_mfma_scale_f32_16x16x128_f8f6f4 v[18:21], v[234:241], v[218:225], v[18:21], v205, v205 op_sel_hi:[0,0,0]
	s_setprio 0
	s_add_i32 s76, s76, 2
	s_add_u32 s66, s66, 0x100
	s_addc_u32 s67, s67, 0
	s_add_u32 s74, s74, 0x100
	s_addc_u32 s75, s75, 0
	s_cmp_gt_u32 s76, 5
	s_barrier
	s_cbranch_scc0 .LBB0_419
	v_mul_f32_e32 v4, 0xbcb8aa3b, v136
	v_mul_f32_e32 v5, 0xbcb8aa3b, v137
	v_exp_f32_e32 v4, v4
	v_exp_f32_e32 v5, v5
	v_mul_f32_e32 v6, 0xbcb8aa3b, v138
	v_mul_f32_e32 v7, 0xbcb8aa3b, v139
	v_exp_f32_e32 v6, v6
	v_exp_f32_e32 v7, v7
	v_med3_f32 v8, v4, s26, v209
	v_med3_f32 v5, v5, s26, v209
	v_mov_b32_e32 v4, v131
	v_cvt_pk_fp8_f32 v4, v8, v5
	v_med3_f32 v5, v6, s26, v209
	v_med3_f32 v6, v7, s26, v209
	v_mul_f32_e32 v7, 0xbcb8aa3b, v134
	v_cvt_pk_fp8_f32 v4, v5, v6 op_sel:[0,0,1]
	v_mul_f32_e32 v5, 0xbcb8aa3b, v132
	v_mul_f32_e32 v6, 0xbcb8aa3b, v133
	v_exp_f32_e32 v5, v5
	v_exp_f32_e32 v6, v6
	v_mul_f32_e32 v8, 0xbcb8aa3b, v135
	v_exp_f32_e32 v7, v7
	v_exp_f32_e32 v8, v8
	v_med3_f32 v9, v5, s26, v209
	v_med3_f32 v6, v6, s26, v209
	v_mov_b32_e32 v5, v131
	v_cvt_pk_fp8_f32 v5, v9, v6
	v_med3_f32 v6, v7, s26, v209
	v_med3_f32 v7, v8, s26, v209
	v_mul_f32_e32 v8, 0xbcb8aa3b, v146
	v_cvt_pk_fp8_f32 v5, v6, v7 op_sel:[0,0,1]
	v_mul_f32_e32 v6, 0xbcb8aa3b, v144
	v_mul_f32_e32 v7, 0xbcb8aa3b, v145
	v_exp_f32_e32 v6, v6
	v_exp_f32_e32 v7, v7
	v_mul_f32_e32 v9, 0xbcb8aa3b, v147
	v_exp_f32_e32 v8, v8
	v_exp_f32_e32 v9, v9
	v_med3_f32 v10, v6, s26, v209
	v_med3_f32 v7, v7, s26, v209
	v_mov_b32_e32 v6, v131
	v_cvt_pk_fp8_f32 v6, v10, v7
	v_med3_f32 v7, v8, s26, v209
	v_med3_f32 v8, v9, s26, v209
	v_mul_f32_e32 v9, 0xbcb8aa3b, v142
	v_cvt_pk_fp8_f32 v6, v7, v8 op_sel:[0,0,1]
	v_mul_f32_e32 v7, 0xbcb8aa3b, v140
	v_mul_f32_e32 v8, 0xbcb8aa3b, v141
	v_exp_f32_e32 v7, v7
	v_exp_f32_e32 v8, v8
	v_mul_f32_e32 v10, 0xbcb8aa3b, v143
	v_exp_f32_e32 v9, v9
	v_exp_f32_e32 v10, v10
	v_med3_f32 v11, v7, s26, v209
	v_med3_f32 v8, v8, s26, v209
	v_mov_b32_e32 v7, v131
	v_cvt_pk_fp8_f32 v7, v11, v8
	s_lshl_b32 s9, s16, 8
	s_mul_i32 s16, s16, 0x1e0000
	s_mul_hi_i32 s9, s9, 0x1e00
	s_add_u32 s16, s53, s16
	v_med3_f32 v8, v9, s26, v209
	v_med3_f32 v9, v10, s26, v209
	s_addc_u32 s9, s57, s9
	s_lshl_b32 s17, s17, 8
	v_cvt_pk_fp8_f32 v7, v8, v9 op_sel:[0,0,1]
	s_ashr_i32 s18, s17, 31
	s_add_u32 s16, s16, s17
	s_addc_u32 s17, s9, s18
	v_mov_b32_e32 v130, v169
	s_nop 15
	s_nop 15
	global_store_dwordx4 v130, v[4:7], s[16:17] offset:1536 nt
	v_lshl_add_u64 v[2:3], s[16:17], 0, v[130:131]
	s_mov_b32 s9, 0x1e000
	v_mul_f32_e32 v4, 0xbcb8aa3b, v118
	v_mul_f32_e32 v5, 0xbcb8aa3b, v119
	v_exp_f32_e32 v4, v4
	v_exp_f32_e32 v5, v5
	v_mul_f32_e32 v6, 0xbcb8aa3b, v120
	v_mul_f32_e32 v7, 0xbcb8aa3b, v121
	v_exp_f32_e32 v6, v6
	v_exp_f32_e32 v7, v7
	v_med3_f32 v8, v4, s26, v209
	v_med3_f32 v5, v5, s26, v209
	v_mov_b32_e32 v4, v131
	v_cvt_pk_fp8_f32 v4, v8, v5
	v_med3_f32 v5, v6, s26, v209
	v_med3_f32 v6, v7, s26, v209
	v_mul_f32_e32 v7, 0xbcb8aa3b, v116
	v_cvt_pk_fp8_f32 v4, v5, v6 op_sel:[0,0,1]
	v_mul_f32_e32 v5, 0xbcb8aa3b, v114
	v_mul_f32_e32 v6, 0xbcb8aa3b, v115
	v_exp_f32_e32 v5, v5
	v_exp_f32_e32 v6, v6
	v_mul_f32_e32 v8, 0xbcb8aa3b, v117
	v_exp_f32_e32 v7, v7
	v_exp_f32_e32 v8, v8
	v_med3_f32 v9, v5, s26, v209
	v_med3_f32 v6, v6, s26, v209
	v_mov_b32_e32 v5, v131
	v_cvt_pk_fp8_f32 v5, v9, v6
	v_med3_f32 v6, v7, s26, v209
	v_med3_f32 v7, v8, s26, v209
	v_mul_f32_e32 v8, 0xbcb8aa3b, v128
	v_cvt_pk_fp8_f32 v5, v6, v7 op_sel:[0,0,1]
	v_mul_f32_e32 v6, 0xbcb8aa3b, v126
	v_mul_f32_e32 v7, 0xbcb8aa3b, v127
	v_exp_f32_e32 v6, v6
	v_exp_f32_e32 v7, v7
	v_mul_f32_e32 v9, 0xbcb8aa3b, v129
	v_exp_f32_e32 v8, v8
	v_exp_f32_e32 v9, v9
	v_med3_f32 v10, v6, s26, v209
	v_med3_f32 v7, v7, s26, v209
	v_mov_b32_e32 v6, v131
	v_cvt_pk_fp8_f32 v6, v10, v7
	v_med3_f32 v7, v8, s26, v209
	v_med3_f32 v8, v9, s26, v209
	v_mul_f32_e32 v9, 0xbcb8aa3b, v124
	v_cvt_pk_fp8_f32 v6, v7, v8 op_sel:[0,0,1]
	v_mul_f32_e32 v7, 0xbcb8aa3b, v122
	v_mul_f32_e32 v8, 0xbcb8aa3b, v123
	v_exp_f32_e32 v7, v7
	v_exp_f32_e32 v8, v8
	v_mul_f32_e32 v10, 0xbcb8aa3b, v125
	v_exp_f32_e32 v9, v9
	v_exp_f32_e32 v10, v10
	v_med3_f32 v11, v7, s26, v209
	v_med3_f32 v8, v8, s26, v209
	v_mov_b32_e32 v7, v131
	v_cvt_pk_fp8_f32 v7, v11, v8
	v_med3_f32 v8, v9, s26, v209
	v_med3_f32 v9, v10, s26, v209
	s_mov_b32 s16, s8
	v_cvt_pk_fp8_f32 v7, v8, v9 op_sel:[0,0,1]
	v_add_co_u32_e32 v8, vcc, s9, v2
	s_mov_b32 s9, 0x3c000
	s_nop 0
	v_addc_co_u32_e32 v9, vcc, 0, v3, vcc
	global_store_dwordx4 v[8:9], v[4:7], off offset:1536 nt
	s_mov_b32 s17, s50
	s_mov_b64 s[68:69], s[10:11]
	v_mul_f32_e32 v4, 0xbcb8aa3b, v106
	v_mul_f32_e32 v5, 0xbcb8aa3b, v107
	v_exp_f32_e32 v4, v4
	v_exp_f32_e32 v5, v5
	v_mul_f32_e32 v6, 0xbcb8aa3b, v108
	v_mul_f32_e32 v7, 0xbcb8aa3b, v109
	v_exp_f32_e32 v6, v6
	v_exp_f32_e32 v7, v7
	v_med3_f32 v8, v4, s26, v209
	v_med3_f32 v5, v5, s26, v209
	v_mov_b32_e32 v4, v131
	v_cvt_pk_fp8_f32 v4, v8, v5
	v_med3_f32 v5, v6, s26, v209
	v_med3_f32 v6, v7, s26, v209
	v_mul_f32_e32 v7, 0xbcb8aa3b, v100
	v_cvt_pk_fp8_f32 v4, v5, v6 op_sel:[0,0,1]
	v_mul_f32_e32 v5, 0xbcb8aa3b, v98
	v_mul_f32_e32 v6, 0xbcb8aa3b, v99
	v_exp_f32_e32 v5, v5
	v_exp_f32_e32 v6, v6
	v_mul_f32_e32 v8, 0xbcb8aa3b, v101
	v_exp_f32_e32 v7, v7
	v_exp_f32_e32 v8, v8
	v_med3_f32 v9, v5, s26, v209
	v_med3_f32 v6, v6, s26, v209
	v_mov_b32_e32 v5, v131
	v_cvt_pk_fp8_f32 v5, v9, v6
	v_med3_f32 v6, v7, s26, v209
	v_med3_f32 v7, v8, s26, v209
	v_mul_f32_e32 v8, 0xbcb8aa3b, v112
	v_cvt_pk_fp8_f32 v5, v6, v7 op_sel:[0,0,1]
	v_mul_f32_e32 v6, 0xbcb8aa3b, v110
	v_mul_f32_e32 v7, 0xbcb8aa3b, v111
	v_exp_f32_e32 v6, v6
	v_exp_f32_e32 v7, v7
	v_mul_f32_e32 v9, 0xbcb8aa3b, v113
	v_exp_f32_e32 v8, v8
	v_exp_f32_e32 v9, v9
	v_med3_f32 v10, v6, s26, v209
	v_med3_f32 v7, v7, s26, v209
	v_mov_b32_e32 v6, v131
	v_cvt_pk_fp8_f32 v6, v10, v7
	v_med3_f32 v7, v8, s26, v209
	v_med3_f32 v8, v9, s26, v209
	v_mul_f32_e32 v9, 0xbcb8aa3b, v104
	v_cvt_pk_fp8_f32 v6, v7, v8 op_sel:[0,0,1]
	v_mul_f32_e32 v7, 0xbcb8aa3b, v102
	v_mul_f32_e32 v8, 0xbcb8aa3b, v103
	v_exp_f32_e32 v7, v7
	v_exp_f32_e32 v8, v8
	v_mul_f32_e32 v10, 0xbcb8aa3b, v105
	v_exp_f32_e32 v9, v9
	v_exp_f32_e32 v10, v10
	v_med3_f32 v11, v7, s26, v209
	v_med3_f32 v8, v8, s26, v209
	v_mov_b32_e32 v7, v131
	v_cvt_pk_fp8_f32 v7, v11, v8
	v_med3_f32 v8, v9, s26, v209
	v_med3_f32 v9, v10, s26, v209
	s_mov_b64 s[66:67], s[14:15]
	v_cvt_pk_fp8_f32 v7, v8, v9 op_sel:[0,0,1]
	v_add_co_u32_e32 v8, vcc, s9, v2
	s_mov_b32 s9, 0x5a000
	s_nop 0
	v_addc_co_u32_e32 v9, vcc, 0, v3, vcc
	global_store_dwordx4 v[8:9], v[4:7], off offset:1536 nt
	s_nop 1
	v_mul_f32_e32 v4, 0xbcb8aa3b, v86
	v_mul_f32_e32 v5, 0xbcb8aa3b, v87
	v_exp_f32_e32 v4, v4
	v_exp_f32_e32 v5, v5
	v_mul_f32_e32 v6, 0xbcb8aa3b, v88
	v_mul_f32_e32 v7, 0xbcb8aa3b, v89
	v_exp_f32_e32 v6, v6
	v_exp_f32_e32 v7, v7
	v_med3_f32 v8, v4, s26, v209
	v_med3_f32 v5, v5, s26, v209
	v_mov_b32_e32 v4, v131
	v_cvt_pk_fp8_f32 v4, v8, v5
	v_med3_f32 v5, v6, s26, v209
	v_med3_f32 v6, v7, s26, v209
	v_mul_f32_e32 v7, 0xbcb8aa3b, v72
	v_cvt_pk_fp8_f32 v4, v5, v6 op_sel:[0,0,1]
	v_mul_f32_e32 v5, 0xbcb8aa3b, v70
	v_mul_f32_e32 v6, 0xbcb8aa3b, v71
	v_exp_f32_e32 v5, v5
	v_exp_f32_e32 v6, v6
	v_mul_f32_e32 v8, 0xbcb8aa3b, v73
	v_exp_f32_e32 v7, v7
	v_exp_f32_e32 v8, v8
	v_med3_f32 v9, v5, s26, v209
	v_med3_f32 v6, v6, s26, v209
	v_mov_b32_e32 v5, v131
	v_cvt_pk_fp8_f32 v5, v9, v6
	v_med3_f32 v6, v7, s26, v209
	v_med3_f32 v7, v8, s26, v209
	v_mul_f32_e32 v8, 0xbcb8aa3b, v96
	v_cvt_pk_fp8_f32 v5, v6, v7 op_sel:[0,0,1]
	v_mul_f32_e32 v6, 0xbcb8aa3b, v94
	v_mul_f32_e32 v7, 0xbcb8aa3b, v95
	v_exp_f32_e32 v6, v6
	v_exp_f32_e32 v7, v7
	v_mul_f32_e32 v9, 0xbcb8aa3b, v97
	v_exp_f32_e32 v8, v8
	v_exp_f32_e32 v9, v9
	v_med3_f32 v10, v6, s26, v209
	v_med3_f32 v7, v7, s26, v209
	v_mov_b32_e32 v6, v131
	v_cvt_pk_fp8_f32 v6, v10, v7
	v_med3_f32 v7, v8, s26, v209
	v_med3_f32 v8, v9, s26, v209
	v_mul_f32_e32 v9, 0xbcb8aa3b, v80
	v_cvt_pk_fp8_f32 v6, v7, v8 op_sel:[0,0,1]
	v_mul_f32_e32 v7, 0xbcb8aa3b, v78
	v_mul_f32_e32 v8, 0xbcb8aa3b, v79
	v_exp_f32_e32 v7, v7
	v_exp_f32_e32 v8, v8
	v_mul_f32_e32 v10, 0xbcb8aa3b, v81
	v_exp_f32_e32 v9, v9
	v_exp_f32_e32 v10, v10
	v_med3_f32 v11, v7, s26, v209
	v_med3_f32 v8, v8, s26, v209
	v_mov_b32_e32 v7, v131
	v_cvt_pk_fp8_f32 v7, v11, v8
	v_med3_f32 v8, v9, s26, v209
	v_med3_f32 v9, v10, s26, v209
	v_cvt_pk_fp8_f32 v7, v8, v9 op_sel:[0,0,1]
	v_add_co_u32_e32 v8, vcc, s9, v2
	s_mov_b32 s9, 0xf0000
	s_nop 0
	v_addc_co_u32_e32 v9, vcc, 0, v3, vcc
	global_store_dwordx4 v[8:9], v[4:7], off offset:1536 nt
	s_nop 1
	v_mul_f32_e32 v4, 0xbcb8aa3b, v82
	v_mul_f32_e32 v5, 0xbcb8aa3b, v83
	v_exp_f32_e32 v4, v4
	v_exp_f32_e32 v5, v5
	v_mul_f32_e32 v6, 0xbcb8aa3b, v84
	v_mul_f32_e32 v7, 0xbcb8aa3b, v85
	v_exp_f32_e32 v6, v6
	v_exp_f32_e32 v7, v7
	v_med3_f32 v8, v4, s26, v209
	v_med3_f32 v5, v5, s26, v209
	v_mov_b32_e32 v4, v131
	v_cvt_pk_fp8_f32 v4, v8, v5
	v_med3_f32 v5, v6, s26, v209
	v_med3_f32 v6, v7, s26, v209
	v_mul_f32_e32 v7, 0xbcb8aa3b, v68
	v_cvt_pk_fp8_f32 v4, v5, v6 op_sel:[0,0,1]
	v_mul_f32_e32 v5, 0xbcb8aa3b, v66
	v_mul_f32_e32 v6, 0xbcb8aa3b, v67
	v_exp_f32_e32 v5, v5
	v_exp_f32_e32 v6, v6
	v_mul_f32_e32 v8, 0xbcb8aa3b, v69
	v_exp_f32_e32 v7, v7
	v_exp_f32_e32 v8, v8
	v_med3_f32 v9, v5, s26, v209
	v_med3_f32 v6, v6, s26, v209
	v_mov_b32_e32 v5, v131
	v_cvt_pk_fp8_f32 v5, v9, v6
	v_med3_f32 v6, v7, s26, v209
	v_med3_f32 v7, v8, s26, v209
	v_mul_f32_e32 v8, 0xbcb8aa3b, v92
	v_cvt_pk_fp8_f32 v5, v6, v7 op_sel:[0,0,1]
	v_mul_f32_e32 v6, 0xbcb8aa3b, v90
	v_mul_f32_e32 v7, 0xbcb8aa3b, v91
	v_exp_f32_e32 v6, v6
	v_exp_f32_e32 v7, v7
	v_mul_f32_e32 v9, 0xbcb8aa3b, v93
	v_exp_f32_e32 v8, v8
	v_exp_f32_e32 v9, v9
	v_med3_f32 v10, v6, s26, v209
	v_med3_f32 v7, v7, s26, v209
	v_mov_b32_e32 v6, v131
	v_cvt_pk_fp8_f32 v6, v10, v7
	v_med3_f32 v7, v8, s26, v209
	v_med3_f32 v8, v9, s26, v209
	v_mul_f32_e32 v9, 0xbcb8aa3b, v76
	v_cvt_pk_fp8_f32 v6, v7, v8 op_sel:[0,0,1]
	v_mul_f32_e32 v7, 0xbcb8aa3b, v74
	v_mul_f32_e32 v8, 0xbcb8aa3b, v75
	v_exp_f32_e32 v7, v7
	v_exp_f32_e32 v8, v8
	v_mul_f32_e32 v10, 0xbcb8aa3b, v77
	v_exp_f32_e32 v9, v9
	v_exp_f32_e32 v10, v10
	v_med3_f32 v11, v7, s26, v209
	v_med3_f32 v8, v8, s26, v209
	v_mov_b32_e32 v7, v131
	v_cvt_pk_fp8_f32 v7, v11, v8
	v_med3_f32 v8, v9, s26, v209
	v_med3_f32 v9, v10, s26, v209
	v_cvt_pk_fp8_f32 v7, v8, v9 op_sel:[0,0,1]
	v_add_co_u32_e32 v8, vcc, s9, v2
	s_mov_b32 s9, 0x10e000
	s_nop 0
	v_addc_co_u32_e32 v9, vcc, 0, v3, vcc
	global_store_dwordx4 v[8:9], v[4:7], off offset:1536 nt
	s_nop 1
	v_mul_f32_e32 v4, 0xbcb8aa3b, v58
	v_mul_f32_e32 v5, 0xbcb8aa3b, v59
	v_exp_f32_e32 v4, v4
	v_exp_f32_e32 v5, v5
	v_mul_f32_e32 v6, 0xbcb8aa3b, v60
	v_mul_f32_e32 v7, 0xbcb8aa3b, v61
	v_exp_f32_e32 v6, v6
	v_exp_f32_e32 v7, v7
	v_med3_f32 v8, v4, s26, v209
	v_med3_f32 v5, v5, s26, v209
	v_mov_b32_e32 v4, v131
	v_cvt_pk_fp8_f32 v4, v8, v5
	v_med3_f32 v5, v6, s26, v209
	v_med3_f32 v6, v7, s26, v209
	v_mul_f32_e32 v7, 0xbcb8aa3b, v52
	v_cvt_pk_fp8_f32 v4, v5, v6 op_sel:[0,0,1]
	v_mul_f32_e32 v5, 0xbcb8aa3b, v50
	v_mul_f32_e32 v6, 0xbcb8aa3b, v51
	v_exp_f32_e32 v5, v5
	v_exp_f32_e32 v6, v6
	v_mul_f32_e32 v8, 0xbcb8aa3b, v53
	v_exp_f32_e32 v7, v7
	v_exp_f32_e32 v8, v8
	v_med3_f32 v9, v5, s26, v209
	v_med3_f32 v6, v6, s26, v209
	v_mov_b32_e32 v5, v131
	v_cvt_pk_fp8_f32 v5, v9, v6
	v_med3_f32 v6, v7, s26, v209
	v_med3_f32 v7, v8, s26, v209
	v_mul_f32_e32 v8, 0xbcb8aa3b, v64
	v_cvt_pk_fp8_f32 v5, v6, v7 op_sel:[0,0,1]
	v_mul_f32_e32 v6, 0xbcb8aa3b, v62
	v_mul_f32_e32 v7, 0xbcb8aa3b, v63
	v_exp_f32_e32 v6, v6
	v_exp_f32_e32 v7, v7
	v_mul_f32_e32 v9, 0xbcb8aa3b, v65
	v_exp_f32_e32 v8, v8
	v_exp_f32_e32 v9, v9
	v_med3_f32 v10, v6, s26, v209
	v_med3_f32 v7, v7, s26, v209
	v_mov_b32_e32 v6, v131
	v_cvt_pk_fp8_f32 v6, v10, v7
	v_med3_f32 v7, v8, s26, v209
	v_med3_f32 v8, v9, s26, v209
	v_mul_f32_e32 v9, 0xbcb8aa3b, v56
	v_cvt_pk_fp8_f32 v6, v7, v8 op_sel:[0,0,1]
	v_mul_f32_e32 v7, 0xbcb8aa3b, v54
	v_mul_f32_e32 v8, 0xbcb8aa3b, v55
	v_exp_f32_e32 v7, v7
	v_exp_f32_e32 v8, v8
	v_mul_f32_e32 v10, 0xbcb8aa3b, v57
	v_exp_f32_e32 v9, v9
	v_exp_f32_e32 v10, v10
	v_med3_f32 v11, v7, s26, v209
	v_med3_f32 v8, v8, s26, v209
	v_mov_b32_e32 v7, v131
	v_cvt_pk_fp8_f32 v7, v11, v8
	v_med3_f32 v8, v9, s26, v209
	v_med3_f32 v9, v10, s26, v209
	v_cvt_pk_fp8_f32 v7, v8, v9 op_sel:[0,0,1]
	v_add_co_u32_e32 v8, vcc, s9, v2
	s_mov_b32 s9, 0x12c000
	s_nop 0
	v_addc_co_u32_e32 v9, vcc, 0, v3, vcc
	global_store_dwordx4 v[8:9], v[4:7], off offset:1536 nt
	s_nop 1
	v_mul_f32_e32 v4, 0xbcb8aa3b, v46
	v_mul_f32_e32 v5, 0xbcb8aa3b, v47
	v_exp_f32_e32 v4, v4
	v_exp_f32_e32 v5, v5
	v_mul_f32_e32 v6, 0xbcb8aa3b, v48
	v_mul_f32_e32 v7, 0xbcb8aa3b, v49
	v_exp_f32_e32 v6, v6
	v_exp_f32_e32 v7, v7
	v_med3_f32 v8, v4, s26, v209
	v_med3_f32 v5, v5, s26, v209
	v_mov_b32_e32 v4, v131
	v_cvt_pk_fp8_f32 v4, v8, v5
	v_med3_f32 v5, v6, s26, v209
	v_med3_f32 v6, v7, s26, v209
	v_mul_f32_e32 v7, 0xbcb8aa3b, v40
	v_cvt_pk_fp8_f32 v4, v5, v6 op_sel:[0,0,1]
	v_mul_f32_e32 v5, 0xbcb8aa3b, v38
	v_mul_f32_e32 v6, 0xbcb8aa3b, v39
	v_exp_f32_e32 v5, v5
	v_exp_f32_e32 v6, v6
	v_mul_f32_e32 v8, 0xbcb8aa3b, v41
	v_exp_f32_e32 v7, v7
	v_exp_f32_e32 v8, v8
	v_med3_f32 v9, v5, s26, v209
	v_med3_f32 v6, v6, s26, v209
	v_mov_b32_e32 v5, v131
	v_cvt_pk_fp8_f32 v5, v9, v6
	v_med3_f32 v6, v7, s26, v209
	v_med3_f32 v7, v8, s26, v209
	v_mul_f32_e32 v8, 0xbcb8aa3b, v44
	v_cvt_pk_fp8_f32 v5, v6, v7 op_sel:[0,0,1]
	v_mul_f32_e32 v6, 0xbcb8aa3b, v42
	v_mul_f32_e32 v7, 0xbcb8aa3b, v43
	v_exp_f32_e32 v6, v6
	v_exp_f32_e32 v7, v7
	v_mul_f32_e32 v9, 0xbcb8aa3b, v45
	v_exp_f32_e32 v8, v8
	v_exp_f32_e32 v9, v9
	v_med3_f32 v10, v6, s26, v209
	v_med3_f32 v7, v7, s26, v209
	v_mov_b32_e32 v6, v131
	v_cvt_pk_fp8_f32 v6, v10, v7
	v_med3_f32 v7, v8, s26, v209
	v_med3_f32 v8, v9, s26, v209
	v_mul_f32_e32 v9, 0xbcb8aa3b, v36
	v_cvt_pk_fp8_f32 v6, v7, v8 op_sel:[0,0,1]
	v_mul_f32_e32 v7, 0xbcb8aa3b, v34
	v_mul_f32_e32 v8, 0xbcb8aa3b, v35
	v_exp_f32_e32 v7, v7
	v_exp_f32_e32 v8, v8
	v_mul_f32_e32 v10, 0xbcb8aa3b, v37
	v_exp_f32_e32 v9, v9
	v_exp_f32_e32 v10, v10
	v_med3_f32 v11, v7, s26, v209
	v_med3_f32 v8, v8, s26, v209
	v_mov_b32_e32 v7, v131
	v_cvt_pk_fp8_f32 v7, v11, v8
	v_med3_f32 v8, v9, s26, v209
	v_med3_f32 v9, v10, s26, v209
	v_cvt_pk_fp8_f32 v7, v8, v9 op_sel:[0,0,1]
	v_add_co_u32_e32 v8, vcc, s9, v2
	s_nop 1
	v_addc_co_u32_e32 v9, vcc, 0, v3, vcc
	global_store_dwordx4 v[8:9], v[4:7], off offset:1536 nt
	v_add_co_u32_e32 v2, vcc, 0x14a000, v2
	s_nop 0
	v_mul_f32_e32 v4, 0xbcb8aa3b, v30
	v_mul_f32_e32 v5, 0xbcb8aa3b, v31
	v_exp_f32_e32 v4, v4
	v_exp_f32_e32 v5, v5
	v_mul_f32_e32 v6, 0xbcb8aa3b, v32
	v_mul_f32_e32 v7, 0xbcb8aa3b, v33
	v_exp_f32_e32 v6, v6
	v_exp_f32_e32 v7, v7
	v_med3_f32 v8, v4, s26, v209
	v_med3_f32 v5, v5, s26, v209
	v_mov_b32_e32 v4, v131
	v_cvt_pk_fp8_f32 v4, v8, v5
	v_med3_f32 v5, v6, s26, v209
	v_med3_f32 v6, v7, s26, v209
	v_mul_f32_e32 v7, 0xbcb8aa3b, v24
	v_cvt_pk_fp8_f32 v4, v5, v6 op_sel:[0,0,1]
	v_mul_f32_e32 v5, 0xbcb8aa3b, v22
	v_mul_f32_e32 v6, 0xbcb8aa3b, v23
	v_exp_f32_e32 v5, v5
	v_exp_f32_e32 v6, v6
	v_mul_f32_e32 v8, 0xbcb8aa3b, v25
	v_exp_f32_e32 v7, v7
	v_exp_f32_e32 v8, v8
	v_med3_f32 v9, v5, s26, v209
	v_med3_f32 v6, v6, s26, v209
	v_mov_b32_e32 v5, v131
	v_cvt_pk_fp8_f32 v5, v9, v6
	v_med3_f32 v6, v7, s26, v209
	v_med3_f32 v7, v8, s26, v209
	v_mul_f32_e32 v8, 0xbcb8aa3b, v28
	v_cvt_pk_fp8_f32 v5, v6, v7 op_sel:[0,0,1]
	v_mul_f32_e32 v6, 0xbcb8aa3b, v26
	v_mul_f32_e32 v7, 0xbcb8aa3b, v27
	v_exp_f32_e32 v6, v6
	v_exp_f32_e32 v7, v7
	v_mul_f32_e32 v9, 0xbcb8aa3b, v29
	v_exp_f32_e32 v8, v8
	v_exp_f32_e32 v9, v9
	v_med3_f32 v10, v6, s26, v209
	v_med3_f32 v7, v7, s26, v209
	v_mov_b32_e32 v6, v131
	v_cvt_pk_fp8_f32 v6, v10, v7
	v_med3_f32 v7, v8, s26, v209
	v_med3_f32 v8, v9, s26, v209
	v_mul_f32_e32 v9, 0xbcb8aa3b, v20
	v_cvt_pk_fp8_f32 v6, v7, v8 op_sel:[0,0,1]
	v_mul_f32_e32 v7, 0xbcb8aa3b, v18
	v_mul_f32_e32 v8, 0xbcb8aa3b, v19
	v_exp_f32_e32 v7, v7
	v_exp_f32_e32 v8, v8
	v_mul_f32_e32 v10, 0xbcb8aa3b, v21
	v_exp_f32_e32 v9, v9
	v_exp_f32_e32 v10, v10
	v_med3_f32 v11, v7, s26, v209
	v_med3_f32 v8, v8, s26, v209
	v_mov_b32_e32 v7, v131
	v_cvt_pk_fp8_f32 v7, v11, v8
	v_med3_f32 v8, v9, s26, v209
	v_med3_f32 v9, v10, s26, v209
	v_addc_co_u32_e32 v3, vcc, 0, v3, vcc
	v_cvt_pk_fp8_f32 v7, v8, v9 op_sel:[0,0,1]
	s_and_b64 vcc, exec, s[6:7]
	global_store_dwordx4 v[2:3], v[4:7], off offset:1536 nt
	s_cbranch_vccz .LBB0_416
	s_waitcnt vmcnt(0)
	s_cmpk_gt_u32 s33, 0xff
	s_cbranch_scc1 .LBB0_423
	s_barrier
